# baseline (speedup 1.0000x reference)
.Lca_spin_2:
	global_load_dword v67, v66, s[0:1] sc1
	global_load_dword v68, v66, s[0:1] offset:4 sc1
	s_waitcnt vmcnt(0)
	v_readfirstlane_b32 s10, v67
	v_readfirstlane_b32 s11, v68
	s_nop 1
	s_min_u32 s10, s10, s11
	s_max_u32 s14, s14, s10
	s_cmp_ge_u32 s14, s13
	s_cbranch_scc1 .Lca_ok_1
	s_add_u32 s15, s15, 1
	s_cmp_lt_u32 s15, 0x400000
	s_cbranch_scc0 .Lca_ok_1
	s_sleep 1
	s_branch .Lca_spin_2
